# v50 with the next-layer weight-conversion split between the grid halves moved from 10240/4224 to 9216/5248 items
# speedup vs baseline: 1.0015x; 1.0015x over previous
; #define LAS __attribute__((address_space(3)))
; __device__ __forceinline__ int opaque_tid() { int t = threadIdx.x; asm volatile("" : "+v"(t)); return t; }
;     __device__ __forceinline__ bool next(int i, Unit& u) const {
;         const long L = (long)i * G + c; if (L >= nwg) return false;
;         int wgid = (int)L; { const int q = nwg / NXCD, r = nwg % NXCD, xcd = wgid % NXCD, off = wgid / NXCD; wgid = (xcd < r ? xcd * (q + 1) : r * (q + 1) + (xcd - r) * q) + off; }
;         const int nig = WGM * nN, gid = wgid / nig, fm = gid * WGM, gsz = (nM - fm) < WGM ? (nM - fm) : WGM;
;         u.pm = fm + ((wgid % nig) % gsz); u.pn = (wgid % nig) / gsz; u.e = 0; u.rows = 256;
;         u.a = A + (size_t)u.pm * tstepA; u.b = Bt + (size_t)u.pn * tstep; return true;
; __device__ __forceinline__ void pj_mfma(const Args& a, LAS unsigned char* lds, int layer) {
;     pg8::DenseOrder So; So.init(a.ws + WS_ACT, a.ws + WS_WIN + (size_t)layer * 3328 * D * 2, NTOK, 3328, D, gridDim.x, blockIdx.x);
;     LAS float* gl = (LAS float*)(lds + SEG_OFF + 256);
;     { const int t_ = opaque_tid(); if (t_ < 256) { const int w = t_ >> 6, i = t_ & 63; const float* gp_ = w == 0 ? a.in[I_QGF] : w == 1 ? a.in[I_KGF] : w == 2 ? a.in[I_QGD] : a.in[I_KGD]; gl[t_] = gp_[layer * 64 + i]; } }
;     __syncthreads();
;     EpiProj E{(bf16_t*)(a.ws + WS_PROJ), gl};
;     pg8::gemm_phase<EpiProj, pg8::DenseOrder>(lds, D, So, E);
;     if ((int)blockIdx.x >= (int)gridDim.x - 32) cumsum_unit(a, lds, blockIdx.x - (gridDim.x - 32));
;     if (layer + 1 < NL) { __syncthreads(); constexpr int I_SPLIT = 10240;
;         const int half = gridDim.x / 2; const bool upper = (int)blockIdx.x >= half;
;         p0_prep(a, lds, layer + 1, upper ? half : 0, upper ? (int)gridDim.x - half : half, upper ? 0 : I_SPLIT, upper ? I_SPLIT : (1 << 30)); }
.LBB0_101:
	s_or_b64 exec, exec, s[0:1]
	s_mov_b32 vcc_lo, 0
	s_nop 1
	v_writelane_b32 v254, vcc_lo, 62
	s_nop 1
	s_waitcnt lgkmcnt(0)
	s_barrier
	s_load_dwordx2 s[92:93], s[54:55], 0xa0
	s_load_dwordx16 s[12:27], s[54:55], 0x20
	s_load_dwordx4 s[0:3], s[54:55], 0x90
	s_movk_i32 s5, 0xd1
	s_mov_b32 s67, 0
	s_waitcnt vmcnt(0)
	v_mbcnt_lo_u32_b32 v1, -1, 0
	v_mbcnt_hi_u32_b32 v199, -1, v1
	s_waitcnt lgkmcnt(0)
	v_writelane_b32 v252, s0, 8
	v_and_b32_e32 v240, 64, v199
	s_mul_hi_u32 s85, s77, 0x600
	v_writelane_b32 v252, s1, 9
	v_writelane_b32 v252, s2, 10
	v_writelane_b32 v252, s3, 11
	s_add_u32 s0, s92, 0x100000
	s_addc_u32 s1, s93, 0
	v_writelane_b32 v252, s0, 12
	s_add_u32 s96, s92, 0xbc00000
	s_addc_u32 s97, s93, 0
	v_writelane_b32 v252, s1, 13
	s_lshl_b32 s0, s61, 3
	s_add_u32 s10, s92, 0x180000
	s_addc_u32 s11, s93, 0
	s_add_u32 s80, s92, 0x7c00000
	s_addc_u32 s81, s93, 0
	v_writelane_b32 v252, s0, 14
	s_add_u32 s0, s92, 0xfc00000
	s_addc_u32 s1, s93, 0
	s_add_u32 s50, s92, 0x18c00000
	s_addc_u32 s51, s93, 0
	s_add_u32 s2, s92, 0xa00000
	s_addc_u32 s3, s93, 0
	v_writelane_b32 v252, s2, 15
	s_cmpk_lt_i32 s61, 0x680
	s_mul_i32 s84, s77, 0x600
	v_writelane_b32 v252, s3, 16
	s_cselect_b64 s[2:3], -1, 0
	v_writelane_b32 v252, s2, 17
	v_mov_b32_e32 v35, 0
	v_add_u32_e32 v241, 64, v240
	v_writelane_b32 v252, s3, 18
	s_ashr_i32 s2, s61, 31
	v_writelane_b32 v252, s2, 19
	s_lshr_b32 s2, s2, 29
	s_add_i32 s3, s61, s2
	s_ashr_i32 s2, s3, 3
	s_and_b32 s3, s3, -8
	s_sub_i32 s3, s61, s3
	s_lshl_b32 s4, s3, 6
	s_cmp_lt_i32 s3, 0
	s_cselect_b32 s5, s5, 0xd0
	s_mul_i32 s5, s5, s3
	s_mulk_i32 s3, 0x41
	s_cselect_b32 s3, s3, s4
	s_add_i32 s5, s5, s2
	s_mul_hi_i32 s4, s5, 0x4ec4ec4f
	s_lshr_b32 s6, s4, 31
	s_ashr_i32 s4, s4, 5
	s_add_i32 s4, s4, s6
	s_mul_i32 s6, s4, 0x68
	s_sub_i32 s5, s5, s6
	s_lshl_b32 s7, s4, 3
	s_bfe_i32 s4, s5, 0x80000
	s_bfe_u32 s4, s4, 0x3000c
	s_add_i32 s6, s5, s4
	s_bfe_i32 s4, s6, 0x80000
	s_and_b32 s6, s6, 0xf8
	s_sub_i32 s5, s5, s6
	s_sext_i32_i16 s8, s4
	s_sext_i32_i8 s5, s5
	s_add_i32 s28, s7, s5
	s_ashr_i32 s5, s8, 3
	v_writelane_b32 v252, s5, 20
	s_mov_b32 s6, s28
	s_ashr_i32 s29, s28, 31
	v_writelane_b32 v252, s6, 21
	s_lshr_b32 s4, s8, 3
	v_xor_b32_e32 v236, 16, v199
	v_writelane_b32 v252, s7, 22
	s_lshl_b64 s[6:7], s[28:29], 19
	s_add_u32 s6, s80, s6
	s_addc_u32 s7, s81, s7
	v_writelane_b32 v252, s6, 23
	s_bfe_i64 s[4:5], s[4:5], 0x100000
	s_lshl_b64 s[4:5], s[4:5], 19
	v_writelane_b32 v252, s7, 24
	v_writelane_b32 v252, s4, 25
	v_xor_b32_e32 v237, 32, v199
	v_mov_b32_e32 v238, 1
	v_writelane_b32 v252, s5, 26
	s_ashr_i32 s4, s77, 31
	v_writelane_b32 v252, s4, 27
	s_sub_i32 s4, s77, 32
	s_cmp_ge_i32 s61, s4
	s_cselect_b64 s[6:7], -1, 0
	v_writelane_b32 v252, s6, 28
	s_sub_i32 s4, s61, s4
	s_and_b32 s5, s4, 3
	v_writelane_b32 v252, s7, 29
	s_ashr_i32 s6, s4, 2
	s_ashr_i32 s7, s6, 31
	s_lshl_b32 s5, s5, 2
	s_add_u32 s5, s10, s5
	v_writelane_b32 v252, s10, 30
	s_addc_u32 s8, s11, 0
	s_lshl_b64 s[6:7], s[6:7], 16
	s_add_u32 s6, s5, s6
	s_addc_u32 s7, s8, s7
	s_add_u32 s28, s92, 0x200000
	s_addc_u32 s29, s93, 0
	s_ashr_i32 s5, s4, 31
	s_lshl_b64 s[4:5], s[4:5], 14
	v_writelane_b32 v252, s11, 31
	s_add_u32 s4, s28, s4
	v_writelane_b32 v252, s6, 32
	s_addc_u32 s5, s29, s5
	s_lshr_b32 s8, s77, 1
	v_writelane_b32 v252, s7, 33
	s_sub_i32 s9, s77, s8
	v_writelane_b32 v252, s4, 34
	s_cmp_lt_i32 s61, s8
	v_mov_b32_e32 v198, 0x358637bd
	v_writelane_b32 v252, s5, 35
	s_cselect_b64 s[4:5], -1, 0
	s_and_b64 s[6:7], s[4:5], exec
	s_cselect_b32 s6, s8, s9
	s_movk_i32 s7, 0x3880
	s_cselect_b32 s10, 0, s8
	s_cselect_b32 s8, 0x2400, 0
	s_cselect_b32 s7, s7, 0x2400
	s_lshl_b32 s6, s6, 3
	v_writelane_b32 v252, s7, 36
	s_cmp_ge_i32 s61, s10
	v_writelane_b32 v252, s6, 37
	s_cselect_b64 s[6:7], -1, 0
	s_or_b64 s[4:5], s[36:37], s[4:5]
	s_load_dwordx8 s[36:43], s[54:55], 0x60
	s_and_b64 s[4:5], s[6:7], s[4:5]
	v_writelane_b32 v252, s4, 38
	v_mov_b32_e32 v201, 1.0
	v_mov_b32_e32 v239, 0x7f800000
	v_writelane_b32 v252, s5, 39
	s_sub_i32 s4, s61, s10
	s_lshl_b32 s4, s4, 3
	s_add_i32 s4, s4, s8
	s_waitcnt lgkmcnt(0)
	s_mov_b64 s[8:9], s[40:41]
	v_writelane_b32 v252, s4, 40
	s_add_u32 s6, s38, 0x400000
	s_mov_b64 s[10:11], s[42:43]
	s_mov_b64 s[4:5], s[36:37]
	v_writelane_b32 v252, s4, 41
	v_mov_b32_e32 v202, 0x3f317218
	v_mov_b32_e32 v242, 0xff800000
	v_writelane_b32 v252, s5, 42
	v_writelane_b32 v252, s6, 43
	v_writelane_b32 v252, s7, 44
	v_writelane_b32 v252, s8, 45
	v_writelane_b32 v252, s9, 46
	v_writelane_b32 v252, s10, 47
	v_writelane_b32 v252, s11, 48
	s_addc_u32 s7, s39, 0
	v_writelane_b32 v252, s6, 49
	s_add_u32 s4, s16, 0xd04000
	s_movk_i32 s74, 0x1ff
	v_writelane_b32 v252, s7, 50
	v_writelane_b32 v252, s12, 51
	s_addc_u32 s5, s17, 0
	s_mov_b32 s76, 0x800000
	v_writelane_b32 v255, s25, 0
	v_writelane_b32 v255, s26, 1
	v_writelane_b32 v255, s27, 2
	v_writelane_b32 v255, s4, 3
	v_writelane_b32 v252, s13, 52
	v_writelane_b32 v252, s14, 53
	v_writelane_b32 v255, s5, 4
	s_add_u32 s4, s92, 0x5b00000
	s_addc_u32 s5, s93, 0
	v_writelane_b32 v255, s4, 5
	v_writelane_b32 v252, s15, 54
	v_writelane_b32 v252, s16, 55
	v_writelane_b32 v255, s5, 6
	s_add_u32 s4, s92, 0x1b00000
	s_addc_u32 s5, s93, 0
	s_add_u32 s82, s92, 0x700000
	v_writelane_b32 v255, s4, 7
	s_addc_u32 s83, s93, 0
	v_writelane_b32 v252, s17, 56
	v_writelane_b32 v255, s5, 8
	s_add_u32 s4, s92, 0x14000
	v_writelane_b32 v255, s4, 9
	s_addc_u32 s4, s93, 0
	s_add_i32 s6, s61, 0x900
	s_cmpk_lt_i32 s61, 0x200
	v_writelane_b32 v255, s4, 10
	s_cselect_b64 s[4:5], -1, 0
	v_writelane_b32 v255, s4, 11
	v_writelane_b32 v252, s18, 57
	v_writelane_b32 v252, s19, 58
	v_writelane_b32 v255, s5, 12
;     ...
;         if (u < AT_NFOX) {
;             const int qb = 15 - (u >> 5), bh = u & 31, b = bh >> 2, h = bh & 3, q0 = qb * 256;
;             const size_t rb = (size_t)b * S;
;             const bf16_t* Kb = proj + ((size_t)(4 + h) * NTOK + rb) * 64;
;             const bf16_t* Vb = proj + ((size_t)(8 + h) * NTOK + rb) * 64;
;             const float* cum = cumall + (size_t)bh * S;
;             const int jhi = 4 * qb + 3;
;             fox_cr = cum[q0]; fox_cv = cum[64 * (lane <= jhi ? lane : jhi) + 63]; fox_cq = cum[q0 + 32 * wid + r32];
;             if (!(dbg & 1)) { FOX_ISSUE(0); FOX_ISSUE(1); FOX_ISSUE(2); }
;             const bf16_t* Q = proj + ((size_t)(0 + h) * NTOK + rb + q0 + 32 * wid + r32) * 64;
; #pragma unroll
;             for (int d0 = 0; d0 < 4; ++d0) qr[d0] = *(const bf16x8*)(Q + d0 * 16 + hi * 8);
;         } else if (u < AT_NFOX + AT_NDIL) {
;             const int v2 = u - AT_NFOX, bh = v2 % 48, rest = v2 / 48, b = bh / 6, h = bh % 6, p = rest >> 4, x = rest & 15;
;             const int dil = p == 0 ? 1 : p == 1 ? 4 : 16, res = x % dil, nb2 = x / dil;
;             const size_t rb = (size_t)b * S;
;             const bf16_t* Kb = proj + ((size_t)(22 + h) * NTOK + rb) * 64;
;             const bf16_t* Vb = proj + ((size_t)(28 + h) * NTOK + rb) * 64;
;             const int mk_base = 256 * nb2 - 128, tt_lo = nb2 == 0 ? 2 : 0;
;             const size_t rs = (size_t)64 * dil;
; #pragma unroll
;     ...
;             if (tid < 256) { const int st = tid - 64; tab[tid] = (st >= 0 && st <= 128) ? relb[t5_bucket(st * dil) * 6 + h] : -INFINITY; }
;             const size_t trow = (size_t)(256 * nb2 + 32 * wid + r32) * dil + res;
;             const bf16_t* Q = proj + ((size_t)(16 + h) * NTOK + rb + trow) * 64;
; #pragma unroll
;             for (int d0 = 0; d0 < 4; ++d0) qr[d0] = *(const bf16x8*)(Q + d0 * 16 + hi * 8);
;         } else {
;             const int v2 = u - AT_NFOX - AT_NDIL, qb = 15 - v2 / 48, bh = v2 % 48, b = bh / 6, h = bh % 6, q0 = qb * 256;
;             const size_t rb = (size_t)b * S;
;             const bf16_t* Kb = proj + ((size_t)(40 + h) * NTOK + rb) * 64;
;             const bf16_t* Vb = proj + ((size_t)(46 + h) * NTOK + rb) * 64;
;             const int jhi = (q0 + 254) >> 6;
;             if (!(dbg & 1)) { SB_ISSUE(0); SB_ISSUE(1); SB_ISSUE(2); }
	s_and_b64 s[4:5], s[4:5], exec
	s_cselect_b32 s13, s61, s6
	s_cmpk_lt_i32 s13, 0xe00
	s_cselect_b64 s[4:5], -1, 0
	v_writelane_b32 v255, s4, 13
	s_cmpk_gt_i32 s13, 0x1ff
	s_mov_b32 s17, s67
	v_writelane_b32 v255, s5, 14
	s_cselect_b64 s[4:5], -1, 0
	v_writelane_b32 v255, s4, 15
	s_cmpk_gt_u32 s13, 0xaff
	v_writelane_b32 v252, s20, 59
	v_writelane_b32 v255, s5, 16
	s_cselect_b64 s[4:5], -1, 0
	v_writelane_b32 v255, s4, 17
	v_writelane_b32 v252, s21, 60
	s_mov_b32 s21, s67
	v_writelane_b32 v255, s5, 18
	s_add_i32 s4, s13, 0xf500
	s_and_b32 s5, s4, 0xffff
	s_mul_i32 s5, s5, 0xaaab
	s_lshr_b32 s5, s5, 21
	s_mul_i32 s6, s5, 48
	s_sub_i32 s4, s4, s6
	s_and_b32 s6, s4, 0xff
	s_mulk_i32 s6, 0xab
	s_bfe_u32 s6, s6, 0x6000a
	s_mul_i32 s7, s6, 6
	s_sub_i32 s4, s4, s7
	s_and_b32 s4, s4, 0xff
	s_lshl_b32 s6, s6, 12
	s_lshl_b32 s4, s4, 15
	s_add_i32 s7, s6, s4
	s_lshl_b32 s7, s7, 7
	s_add_i32 s8, s7, 0xb800000
	s_add_u32 s8, s96, s8
	s_addc_u32 s9, s97, 0
	s_add_i32 s7, s7, 0xa000000
	s_add_u32 s7, s96, s7
	s_addc_u32 s10, s97, 0
	s_lshl_b32 s11, s5, 14
	s_sub_i32 s12, 0x3f000, s11
	s_lshl_b32 s12, s12, 1
	s_add_u32 s14, s7, s12
	s_addc_u32 s15, s10, 0
	v_writelane_b32 v255, s14, 19
	v_writelane_b32 v252, s22, 61
	v_writelane_b32 v252, s23, 62
	v_writelane_b32 v255, s15, 20
	s_add_u32 s14, s8, s12
	s_addc_u32 s15, s9, 0
	s_sub_i32 s12, 0x3e000, s11
	v_writelane_b32 v255, s14, 21
	s_lshl_b32 s12, s12, 1
	v_writelane_b32 v252, s24, 63
	v_writelane_b32 v255, s15, 22
	s_add_u32 s14, s7, s12
	s_addc_u32 s15, s10, 0
	v_writelane_b32 v255, s14, 23
	s_movk_i32 s56, 0x7f
	s_mov_b32 s57, 0xff800000
	v_writelane_b32 v255, s15, 24
	s_add_u32 s14, s8, s12
	s_addc_u32 s15, s9, 0
	s_sub_i32 s11, 0x3d000, s11
	v_writelane_b32 v255, s14, 25
	s_lshl_b32 s11, s11, 1
	s_mov_b32 s65, 0xc2ce8ed0
	v_writelane_b32 v255, s15, 26
	s_add_u32 s14, s7, s11
	s_addc_u32 s15, s10, 0
	s_add_u32 s8, s8, s11
	s_addc_u32 s9, s9, 0
	s_lshl_b32 s5, s5, 8
	s_sub_i32 s4, s4, s5
	s_add_i32 s5, s13, 0xfe00
	s_add_i32 s4, s4, s6
	s_and_b32 s6, s5, 0xffff
	s_mul_i32 s6, s6, 0xaaab
	s_lshr_b32 s7, s6, 21
	s_mul_i32 s7, s7, 48
	s_sub_i32 s5, s5, s7
	v_writelane_b32 v255, s14, 27
	s_and_b32 s7, s5, 0xff
	s_mulk_i32 s7, 0xab
	v_writelane_b32 v255, s15, 28
	v_writelane_b32 v255, s8, 29
	s_bfe_u32 s7, s7, 0x6000a
	s_add_i32 s4, s4, 0x110f00
	v_writelane_b32 v255, s9, 30
	s_mul_i32 s8, s7, 6
	s_sub_i32 s5, s5, s8
	s_and_b32 s5, s5, 0xff
	s_lshl_b32 s7, s7, 12
	s_lshl_b32 s8, s5, 15
	s_add_i32 s7, s7, s8
	v_writelane_b32 v255, s4, 31
	s_bfe_u32 s4, s6, 0x40015
	s_lshl_b32 s6, s7, 7
	s_add_u32 s6, s96, s6
	s_addc_u32 s8, s97, 0
	s_add_u32 s9, s6, 0x5800000
	s_addc_u32 s10, s8, 0
	s_add_u32 s6, s6, 0x7000000
	s_addc_u32 s8, s8, 0
	s_lshl_b32 s11, s4, 7
	s_or_b32 s12, s11, 0x60000
	s_add_u32 s14, s9, s12
	s_addc_u32 s15, s10, 0
	v_writelane_b32 v255, s14, 32
	s_mov_b64 s[44:45], -1
	s_mov_b64 s[86:87], 0x800
	v_writelane_b32 v255, s15, 33
	s_add_u32 s14, s6, s12
	s_addc_u32 s15, s8, 0
	v_writelane_b32 v255, s14, 34
	s_or_b32 s12, s11, 0x40000
	s_mov_b32 s60, 0xbfb8aa3b
	v_writelane_b32 v255, s15, 35
	s_add_u32 s14, s9, s12
	s_addc_u32 s15, s10, 0
	v_writelane_b32 v255, s14, 36
	s_mov_b64 s[88:89], 0x80
	s_mov_b64 s[94:95], 0x100
	v_writelane_b32 v255, s15, 37
	s_add_u32 s14, s6, s12
	s_addc_u32 s15, s8, 0
	v_writelane_b32 v255, s14, 38
	s_or_b32 s12, s11, 0x20000
	s_mov_b32 s62, s67
	v_writelane_b32 v255, s15, 39
	s_add_u32 s14, s9, s12
	s_addc_u32 s15, s10, 0
	v_writelane_b32 v255, s14, 40
	s_nop 1
	v_writelane_b32 v255, s15, 41
	s_add_u32 s14, s6, s12
	s_addc_u32 s15, s8, 0
	v_writelane_b32 v255, s14, 42
	s_nop 1
	v_writelane_b32 v255, s15, 43
	s_add_u32 s14, s9, s11
	s_addc_u32 s15, s10, 0
	v_writelane_b32 v255, s14, 44
	s_add_u32 s10, s6, s11
	s_addc_u32 s11, s8, 0
	v_writelane_b32 v255, s15, 45
	s_lshl_b32 s5, s5, 2
	v_writelane_b32 v255, s10, 46
	s_add_i32 s5, s5, 0
	s_add_i32 s5, s5, 0x21f00
	v_writelane_b32 v255, s11, 47
	v_writelane_b32 v255, s5, 48
	s_ashr_i32 s5, s13, 5
	s_or_b32 s4, s7, s4
	s_sub_i32 s5, 15, s5
	s_lshl_b32 s6, s13, 10
	s_and_b32 s7, s13, 31
	s_and_b32 s6, s6, 0x7000
	s_lshl_b32 s7, s7, 14
	s_or_b32 s14, s4, 0x80000
	s_and_b32 s8, s13, 3
	s_lshl_b32 s16, s5, 8
	s_add_u32 s18, s28, s7
	s_addc_u32 s19, s29, 0
	s_lshl_b32 s7, s5, 2
	v_writelane_b32 v255, s13, 49
	s_or_b32 s20, s7, 3
	s_lshl_b64 s[4:5], s[16:17], 2
	v_writelane_b32 v255, s28, 50
	s_add_u32 s4, s18, s4
	v_writelane_b32 v255, s29, 51
	s_addc_u32 s5, s19, s5
	v_writelane_b32 v255, s4, 52
	s_mov_b32 s15, s67
	s_nop 0
	v_writelane_b32 v255, s5, 53
	s_lshl_b32 s4, s8, 22
	s_lshl_b32 s5, s6, 7
	s_or_b32 s4, s5, s4
	s_add_u32 s4, s96, s4
	s_addc_u32 s5, s97, 0
	s_add_u32 s9, s4, 0x2000000
	s_addc_u32 s10, s5, 0
	s_add_u32 s11, s4, 0x1000000
	s_addc_u32 s12, s5, 0
	s_lshl_b64 s[4:5], s[20:21], 13
	s_add_u32 s22, s11, s4
	s_addc_u32 s23, s12, s5
	v_writelane_b32 v255, s22, 54
	s_add_u32 s4, s9, s4
	s_addc_u32 s5, s10, s5
	v_writelane_b32 v255, s23, 55
	v_writelane_b32 v255, s4, 56
	s_lshl_b32 s66, s20, 6
	s_nop 0
	v_writelane_b32 v255, s5, 57
	s_mov_b32 s4, s20
	v_writelane_b32 v255, s4, 58
	s_nop 1
	v_writelane_b32 v255, s5, 59
	s_lshl_b64 s[4:5], s[66:67], 2
	s_add_u32 s4, s18, s4
	s_addc_u32 s5, s19, s5
	v_writelane_b32 v255, s4, 60
; #define LAS __attribute__((address_space(3)))
; #define FOX_ISSUE(i) do { const int j_ = jhi - (i), bf_ = (i) & 3; dma_kv(lds, bf_, Kb + (size_t)j_ * 4096, Vb + (size_t)j_ * 4096, 64, wid, lane); \
;         glds4(cum + j_ * 64 + lane, (unsigned)__builtin_amdgcn_readfirstlane(l0 + L_CK + bf_ * 256)); } while (0)
;     ...
;     bf16x8 qr[4];
;     float fox_cr = 0.f, fox_cv = 0.f, fox_cq = 0.f;
;     auto prologue = [&](int u) {
;         if (!UNIT_ON(u)) return;
;         int lane = tid & 63; asm volatile("" : "+v"(lane));
;         const int r32 = lane & 31, hi = lane >> 5;
;         if (u < AT_NFOX) {
;             const int qb = 15 - (u >> 5), bh = u & 31, b = bh >> 2, h = bh & 3, q0 = qb * 256;
;             const size_t rb = (size_t)b * S;
;             const bf16_t* Kb = proj + ((size_t)(4 + h) * NTOK + rb) * 64;
;             const bf16_t* Vb = proj + ((size_t)(8 + h) * NTOK + rb) * 64;
;             const float* cum = cumall + (size_t)bh * S;
;             const int jhi = 4 * qb + 3;
;             fox_cr = cum[q0]; fox_cv = cum[64 * (lane <= jhi ? lane : jhi) + 63]; fox_cq = cum[q0 + 32 * wid + r32];
;             if (!(dbg & 1)) { FOX_ISSUE(0); FOX_ISSUE(1); FOX_ISSUE(2); }
;             const bf16_t* Q = proj + ((size_t)(0 + h) * NTOK + rb + q0 + 32 * wid + r32) * 64;
; #pragma unroll
;             for (int d0 = 0; d0 < 4; ++d0) qr[d0] = *(const bf16x8*)(Q + d0 * 16 + hi * 8);
; __device__ __forceinline__ void op_mfma(const Args& a, LAS unsigned char* lds, int layer, bf16_t* outp = nullptr) {
;     pg8::DenseOrder So; So.init(a.ws + WS_ACT, a.ws + WS_WOUT + (size_t)layer * D * D * 2, NTOK, D, D, gridDim.x, blockIdx.x, (size_t)256 * 128);
;     bf16_t* xb = (bf16_t*)(a.ws + WS_XB);
;     EpiOut E{layer == 0 ? a.in[I_X] : nullptr, xb, outp ? outp : xb, (const float*)(a.ws + WS_MOD) + (size_t)layer * NB * 6144 + 2048};
;     pg8::gemm_phase<EpiOut, pg8::DenseOrder>(lds, D, So, E, 128u, (size_t)NTOK * 128);
	s_or_b32 s66, s7, 2
	s_nop 0
	v_writelane_b32 v255, s5, 61
	s_lshl_b64 s[4:5], s[66:67], 13
	s_add_u32 s20, s11, s4
	s_addc_u32 s21, s12, s5
	s_add_u32 s4, s9, s4
	s_addc_u32 s5, s10, s5
	v_writelane_b32 v253, s4, 0
	s_lshl_b32 s66, s66, 6
	v_writelane_b32 v255, s20, 62
	v_writelane_b32 v253, s5, 1
	s_lshl_b64 s[4:5], s[66:67], 2
	s_add_u32 s4, s18, s4
	s_addc_u32 s5, s19, s5
	v_writelane_b32 v253, s4, 2
	s_or_b32 s66, s7, 1
	v_writelane_b32 v255, s21, 63
	v_writelane_b32 v253, s5, 3
	s_lshl_b64 s[4:5], s[66:67], 13
	s_add_u32 s20, s11, s4
	s_addc_u32 s21, s12, s5
	v_writelane_b32 v253, s20, 4
	s_add_u32 s4, s9, s4
	s_addc_u32 s5, s10, s5
	v_writelane_b32 v253, s21, 5
	v_writelane_b32 v253, s4, 6
	s_lshl_b32 s66, s66, 6
	s_mov_b32 s9, s67
	v_writelane_b32 v253, s5, 7
	s_lshl_b64 s[4:5], s[66:67], 2
	s_add_u32 s4, s18, s4
	v_writelane_b32 v253, s18, 8
	s_addc_u32 s5, s19, s5
	s_nop 0
	v_writelane_b32 v253, s19, 9
	v_writelane_b32 v253, s4, 10
	s_nop 1
	v_writelane_b32 v253, s5, 11
	s_lshl_b32 s4, s8, 15
	s_or_b32 s4, s6, s4
	s_mov_b32 s6, s16
	v_writelane_b32 v253, s6, 12
	s_add_i32 s4, s4, s16
	s_mov_b32 s8, s77
	v_writelane_b32 v253, s7, 13
	s_mov_b32 s6, s61
	s_mov_b32 s7, s67
	v_writelane_b32 v253, s4, 14
	s_lshl_b64 s[4:5], s[6:7], 9
	s_lshl_b64 s[70:71], s[8:9], 9
	v_writelane_b32 v253, s4, 15
	s_nop 1
	v_writelane_b32 v253, s5, 16
	s_add_u32 s4, s92, 0x8c00000
	s_addc_u32 s5, s93, 0
	v_writelane_b32 v253, s4, 17
	s_nop 1
	v_writelane_b32 v253, s5, 18
	s_add_u32 s4, s92, 0x1700000
	v_writelane_b32 v253, s4, 19
	s_addc_u32 s4, s93, 0
	v_writelane_b32 v253, s4, 20
	s_add_u32 s4, s92, 0x10000
	v_writelane_b32 v253, s4, 21
	s_addc_u32 s4, s93, 0
	v_writelane_b32 v253, s4, 22
	s_add_u32 s4, s92, 0x300000
	s_addc_u32 s5, s93, 0
	v_writelane_b32 v253, s4, 23
	s_nop 1
	v_writelane_b32 v253, s5, 24
	s_add_u32 s4, s92, 0x500000
	s_addc_u32 s5, s93, 0
	v_writelane_b32 v253, s4, 25
	s_cmpk_lt_i32 s61, 0x100
	s_nop 0
	v_writelane_b32 v253, s5, 26
	s_cselect_b64 s[4:5], -1, 0
	v_writelane_b32 v253, s4, 27
	s_nop 1
	v_writelane_b32 v253, s5, 28
	s_add_u32 s4, s92, 0x14400000
	s_addc_u32 s5, s93, 0
	v_writelane_b32 v253, s4, 29
	s_nop 1
	v_writelane_b32 v253, s5, 30
	s_add_i32 s4, s77, s61
	v_writelane_b32 v253, s4, 31
	s_add_u32 s4, s92, 0x7c00080
	s_addc_u32 s5, s93, 0
	s_add_i32 s2, s3, s2
	s_ashr_i32 s3, s2, 31
	s_lshr_b32 s3, s3, 27
	v_writelane_b32 v253, s4, 32
	s_add_i32 s3, s2, s3
	s_nop 0
	v_writelane_b32 v253, s5, 33
	s_and_b32 s4, s3, 0xffe0
	s_sub_i32 s2, s2, s4
	s_bfe_i32 s4, s2, 0x80000
	s_bfe_u32 s4, s4, 0x3000c
	s_add_i32 s4, s2, s4
	s_and_b32 s5, s4, 0xf8
	s_sub_i32 s2, s2, s5
	s_ashr_i32 s3, s3, 5
	s_bfe_i32 s4, s4, 0x80000
	s_lshl_b32 s3, s3, 3
	s_sext_i32_i16 s4, s4
	s_sext_i32_i8 s2, s2
	s_add_i32 s10, s3, s2
	s_ashr_i32 s2, s4, 3
	v_writelane_b32 v253, s2, 34
	s_lshr_b32 s2, s4, 3
	s_mov_b32 s4, s10
	s_ashr_i32 s11, s10, 31
	v_writelane_b32 v253, s4, 35
	s_nop 1
	v_writelane_b32 v253, s5, 36
	s_lshl_b64 s[4:5], s[10:11], 15
	s_add_u32 s4, s80, s4
	s_addc_u32 s5, s81, s5
	v_writelane_b32 v253, s14, 37
	s_bfe_i64 s[2:3], s[2:3], 0x100000
	s_lshl_b64 s[2:3], s[2:3], 19
	v_writelane_b32 v253, s15, 38
	v_writelane_b32 v253, s2, 39
	s_nop 1
	v_writelane_b32 v253, s3, 40
	s_add_u32 s2, s4, 0x4000
	s_addc_u32 s3, s5, 0
	v_writelane_b32 v253, s2, 41
	s_nop 1
	v_writelane_b32 v253, s3, 42
	s_add_u32 s2, s4, 0x400000
	v_writelane_b32 v253, s4, 43
	s_addc_u32 s3, s5, 0
	s_lshl_b64 s[52:53], s[8:9], 10
	v_writelane_b32 v253, s5, 44
	v_writelane_b32 v253, s2, 45
	s_add_i32 s64, 0, 0x13000
	s_nop 0
	v_writelane_b32 v253, s3, 46
	s_lshl_b32 s2, s61, 7
	v_writelane_b32 v253, s2, 47
	s_lshl_b32 s2, s77, 7
	v_writelane_b32 v253, s2, 48
	s_mul_i32 s2, s77, 0x3000
	v_writelane_b32 v253, s2, 49
	s_add_i32 s2, 0, 0x21c20
	v_writelane_b32 v253, s2, 50
	s_add_i32 s2, 0, 0x21c24
	v_writelane_b32 v253, s2, 51
	s_add_i32 s2, 0, 0x21000
	v_writelane_b32 v253, s2, 52
	s_add_i32 s2, 0, 0x21100
	v_writelane_b32 v253, s2, 53
	s_add_i32 s2, 0, 0x21200
	v_writelane_b32 v253, s2, 54
	s_add_i32 s2, 0, 0x21504
	v_writelane_b32 v253, s2, 55
	s_add_i32 s2, 0, 0x15040
	v_writelane_b32 v253, s2, 56
	s_add_i32 s2, 0, 0x15000
	v_writelane_b32 v253, s2, 57
	s_add_i32 s2, 0, 0x21e80
	v_writelane_b32 v253, s2, 58
	s_add_i32 s2, 0, 0x21e10
	v_writelane_b32 v253, s2, 59
	s_add_i32 s2, 0, 0x21e20
	v_writelane_b32 v253, s2, 60
	s_add_i32 s2, 0, 0x21e30
	v_writelane_b32 v253, s2, 61
	v_writelane_b32 v253, s54, 62
	s_load_dwordx2 s[4:5], s[54:55], 0x0
	s_mov_b32 s3, 0x42b17218
	v_writelane_b32 v253, s55, 63
	s_waitcnt lgkmcnt(0)
	v_writelane_b32 v254, s4, 0
	s_nop 1
	v_writelane_b32 v254, s5, 1
	s_lshl_b64 s[4:5], s[8:9], 13
	v_writelane_b32 v254, s4, 2
	s_nop 1
	v_writelane_b32 v254, s5, 3
	v_writelane_b32 v254, s6, 4
	s_lshl_b64 s[4:5], s[6:7], 12
	s_nop 0
	v_writelane_b32 v254, s7, 5
	v_writelane_b32 v254, s4, 6
	s_nop 1
	v_writelane_b32 v254, s5, 7
	s_lshl_b64 s[4:5], s[8:9], 14
	v_writelane_b32 v254, s4, 8
	s_nop 1
	v_writelane_b32 v254, s5, 9
	v_writelane_b32 v254, s8, 10
	s_lshl_b64 s[4:5], s[8:9], 12
	s_nop 0
	v_writelane_b32 v254, s9, 11
	v_writelane_b32 v254, s4, 12
	s_nop 1
	v_writelane_b32 v254, s5, 13
	v_writelane_b32 v254, s82, 14
	s_nop 1
	v_writelane_b32 v254, s83, 15
	s_branch .LBB0_104
